# grid barrier spin loops: s_sleep 6 instead of s_sleep 1 (less polling traffic); on top of router loop rewrite
# speedup vs baseline: 1.0017x; 1.0017x over previous
; __device__ __forceinline__ unsigned xb_ld(unsigned* p)              { return __hip_atomic_load(p, __ATOMIC_RELAXED, __HIP_MEMORY_SCOPE_AGENT); }
; __device__ __forceinline__ void xcd_barrier_complete(unsigned* bar, unsigned x, unsigned& nloc, unsigned& nx) {
;     const unsigned G = gridDim.x * gridDim.y * gridDim.z;
;     unsigned sum, cnt, mine, sp = 0u;
;     for (;;) {
;         sum = 0u; cnt = 0u; mine = 0u;
; #pragma unroll
;         for (unsigned j = 0; j < 16; ++j) { const unsigned c = xb_ld(&bar[XB_XCNT(j)]); sum += c; cnt += (c > 0u) ? 1u : 0u; mine = (j == x) ? c : mine; }
;         if (sum == G) break;
;         __builtin_amdgcn_s_sleep(1);
;         if ((++sp & 255u) == 0u) { if (xb_ld(&bar[XB_TMO])) break; if (sp > XB_SPIN_CAP) { atomicAdd(&bar[XB_TMO], 1u); break; } }
;     }
.LBB0_153:
	global_load_dword v15, v16, s[6:7] sc1
	global_load_dword v0, v16, s[8:9] sc1
	global_load_dword v1, v16, s[10:11] sc1
	global_load_dword v2, v16, s[12:13] sc1
	global_load_dword v3, v16, s[16:17] sc1
	global_load_dword v4, v16, s[18:19] sc1
	global_load_dword v5, v16, s[20:21] sc1
	global_load_dword v6, v16, s[22:23] sc1
	global_load_dword v7, v16, s[24:25] sc1
	global_load_dword v8, v16, s[26:27] sc1
	global_load_dword v9, v16, s[30:31] sc1
	global_load_dword v10, v16, s[34:35] sc1
	global_load_dword v11, v16, s[36:37] sc1
	global_load_dword v12, v16, s[38:39] sc1
	global_load_dword v13, v16, s[40:41] sc1
	global_load_dword v14, v16, s[42:43] sc1
	s_mov_b64 s[44:45], -1
	s_mov_b64 s[46:47], -1
	s_waitcnt vmcnt(14)
	v_add_u32_e32 v17, v0, v15
	s_waitcnt vmcnt(13)
	v_add_u32_e32 v17, v17, v1
	s_waitcnt vmcnt(12)
	v_add_u32_e32 v17, v17, v2
	s_waitcnt vmcnt(11)
	v_add_u32_e32 v17, v17, v3
	s_waitcnt vmcnt(10)
	v_add_u32_e32 v17, v17, v4
	s_waitcnt vmcnt(9)
	v_add_u32_e32 v17, v17, v5
	s_waitcnt vmcnt(8)
	v_add_u32_e32 v17, v17, v6
	s_waitcnt vmcnt(7)
	v_add_u32_e32 v17, v17, v7
	s_waitcnt vmcnt(6)
	v_add_u32_e32 v17, v17, v8
	s_waitcnt vmcnt(5)
	v_add_u32_e32 v17, v17, v9
	s_waitcnt vmcnt(4)
	v_add_u32_e32 v17, v17, v10
	s_waitcnt vmcnt(3)
	v_add_u32_e32 v17, v17, v11
	s_waitcnt vmcnt(2)
	v_add_u32_e32 v17, v17, v12
	s_waitcnt vmcnt(1)
	v_add_u32_e32 v17, v17, v13
	s_waitcnt vmcnt(0)
	v_add_u32_e32 v17, v17, v14
	v_cmp_eq_u32_e32 vcc, s50, v17
	s_cbranch_vccnz .LBB0_152
	s_and_b32 s44, s51, 0xff
	s_cmp_eq_u32 s44, 0
	s_mov_b64 s[44:45], -1
	s_mov_b64 s[48:49], -1
	s_sleep 6
	s_cbranch_scc1 .LBB0_157
	s_and_b64 vcc, exec, s[48:49]
	s_cbranch_vccz .LBB0_152

; __device__ __forceinline__ unsigned xb_ld(unsigned* p)              { return __hip_atomic_load(p, __ATOMIC_RELAXED, __HIP_MEMORY_SCOPE_AGENT); }
; __device__ __forceinline__ unsigned xb_add(unsigned* p, unsigned v) { return __hip_atomic_fetch_add(p, v, __ATOMIC_RELAXED, __HIP_MEMORY_SCOPE_AGENT); }
; #define XB_SPIN(cond, bar) do { unsigned _sp = 0; while (cond) { __builtin_amdgcn_s_sleep(1); \
;     if ((++_sp & 255u) == 0u) { if (xb_ld(&(bar)[XB_TMO])) break; if (_sp > XB_SPIN_CAP) { atomicAdd(&(bar)[XB_TMO], 1u); break; } } } } while (0)
; __device__ __forceinline__ void xcd_barrier(const XcdBarrier& b) {
;     ...
;             else XB_SPIN(xb_ld(&bar[XB_TOPGEN]) == tg, bar);
;             __builtin_amdgcn_fence(__ATOMIC_ACQUIRE, "agent");
;             xb_add(&bar[XB_XGEN(b.x)], 1u);
;             asm volatile("s_waitcnt vmcnt(0)" ::: "memory");
;         } else {
;             XB_SPIN(xb_ld(&bar[XB_XGEN(b.x)]) == gen, bar);
.LBB0_171:
	s_and_b32 s22, s26, 0xff
	s_mov_b64 s[20:21], -1
	s_cmp_lg_u32 s22, 0
	s_mov_b64 s[24:25], -1
	s_sleep 6
	s_cbranch_scc0 .LBB0_174
	s_and_b64 vcc, exec, s[24:25]
	s_cbranch_vccz .LBB0_170

; __device__ __forceinline__ unsigned xb_ld(unsigned* p)              { return __hip_atomic_load(p, __ATOMIC_RELAXED, __HIP_MEMORY_SCOPE_AGENT); }
; __device__ __forceinline__ unsigned xb_add(unsigned* p, unsigned v) { return __hip_atomic_fetch_add(p, v, __ATOMIC_RELAXED, __HIP_MEMORY_SCOPE_AGENT); }
; #define XB_SPIN(cond, bar) do { unsigned _sp = 0; while (cond) { __builtin_amdgcn_s_sleep(1); \
;     if ((++_sp & 255u) == 0u) { if (xb_ld(&(bar)[XB_TMO])) break; if (_sp > XB_SPIN_CAP) { atomicAdd(&(bar)[XB_TMO], 1u); break; } } } } while (0)
; __device__ __forceinline__ void xcd_barrier(const XcdBarrier& b) {
;     ...
;             else XB_SPIN(xb_ld(&bar[XB_TOPGEN]) == tg, bar);
;             __builtin_amdgcn_fence(__ATOMIC_ACQUIRE, "agent");
;             xb_add(&bar[XB_XGEN(b.x)], 1u);
;             asm volatile("s_waitcnt vmcnt(0)" ::: "memory");
;         } else {
;             XB_SPIN(xb_ld(&bar[XB_XGEN(b.x)]) == gen, bar);
.LBB0_188:
	s_and_b32 s20, s26, 0xff
	s_cmp_lg_u32 s20, 0
	s_mov_b64 s[22:23], -1
	s_sleep 6
	s_cbranch_scc0 .LBB0_191
	s_mov_b64 s[24:25], -1
	s_and_b64 vcc, exec, s[22:23]
	s_cbranch_vccz .LBB0_187

; __device__ __forceinline__ unsigned xb_ld(unsigned* p)              { return __hip_atomic_load(p, __ATOMIC_RELAXED, __HIP_MEMORY_SCOPE_AGENT); }
; __device__ __forceinline__ void xcd_barrier_complete(unsigned* bar, unsigned x, unsigned& nloc, unsigned& nx) {
;     const unsigned G = gridDim.x * gridDim.y * gridDim.z;
;     unsigned sum, cnt, mine, sp = 0u;
;     for (;;) {
;         sum = 0u; cnt = 0u; mine = 0u;
; #pragma unroll
;         for (unsigned j = 0; j < 16; ++j) { const unsigned c = xb_ld(&bar[XB_XCNT(j)]); sum += c; cnt += (c > 0u) ? 1u : 0u; mine = (j == x) ? c : mine; }
;         if (sum == G) break;
;         __builtin_amdgcn_s_sleep(1);
;         if ((++sp & 255u) == 0u) { if (xb_ld(&bar[XB_TMO])) break; if (sp > XB_SPIN_CAP) { atomicAdd(&bar[XB_TMO], 1u); break; } }
;     }
.LBB0_263:
	v_readlane_b32 s4, v249, 9
	v_readlane_b32 s5, v249, 10
	s_mov_b64 s[10:11], -1
	s_nop 3
	global_load_dword v0, v1, s[4:5] sc1
	v_readlane_b32 s4, v249, 11
	v_readlane_b32 s5, v249, 12
	s_nop 4
	global_load_dword v2, v1, s[4:5] sc1
	v_readlane_b32 s4, v249, 13
	v_readlane_b32 s5, v249, 14
	s_waitcnt vmcnt(0)
	v_add_u32_e32 v17, v2, v0
	s_nop 2
	global_load_dword v3, v1, s[4:5] sc1
	v_readlane_b32 s4, v249, 15
	v_readlane_b32 s5, v249, 16
	s_waitcnt vmcnt(0)
	v_add_u32_e32 v17, v17, v3
	s_nop 2
	global_load_dword v4, v1, s[4:5] sc1
	v_readlane_b32 s4, v249, 17
	v_readlane_b32 s5, v249, 18
	s_waitcnt vmcnt(0)
	v_add_u32_e32 v17, v17, v4
	s_nop 2
	global_load_dword v5, v1, s[4:5] sc1
	v_readlane_b32 s4, v249, 19
	v_readlane_b32 s5, v249, 20
	s_waitcnt vmcnt(0)
	v_add_u32_e32 v17, v17, v5
	s_nop 2
	global_load_dword v6, v1, s[4:5] sc1
	v_readlane_b32 s4, v249, 21
	v_readlane_b32 s5, v249, 22
	s_waitcnt vmcnt(0)
	v_add_u32_e32 v17, v17, v6
	s_nop 2
	global_load_dword v7, v1, s[4:5] sc1
	v_readlane_b32 s4, v249, 23
	v_readlane_b32 s5, v249, 24
	s_waitcnt vmcnt(0)
	v_add_u32_e32 v17, v17, v7
	s_nop 2
	global_load_dword v8, v1, s[4:5] sc1
	v_readlane_b32 s4, v249, 25
	v_readlane_b32 s5, v249, 26
	s_waitcnt vmcnt(0)
	v_add_u32_e32 v17, v17, v8
	s_nop 2
	global_load_dword v9, v1, s[4:5] sc1
	v_readlane_b32 s4, v249, 27
	v_readlane_b32 s5, v249, 28
	s_waitcnt vmcnt(0)
	v_add_u32_e32 v17, v17, v9
	s_nop 2
	global_load_dword v10, v1, s[4:5] sc1
	v_readlane_b32 s4, v249, 29
	v_readlane_b32 s5, v249, 30
	s_waitcnt vmcnt(0)
	v_add_u32_e32 v17, v17, v10
	s_nop 2
	global_load_dword v11, v1, s[4:5] sc1
	v_readlane_b32 s4, v249, 31
	v_readlane_b32 s5, v249, 32
	s_waitcnt vmcnt(0)
	v_add_u32_e32 v17, v17, v11
	s_nop 2
	global_load_dword v12, v1, s[4:5] sc1
	v_readlane_b32 s4, v249, 33
	v_readlane_b32 s5, v249, 34
	s_waitcnt vmcnt(0)
	v_add_u32_e32 v17, v17, v12
	s_nop 2
	global_load_dword v13, v1, s[4:5] sc1
	v_readlane_b32 s4, v249, 35
	v_readlane_b32 s5, v249, 36
	s_waitcnt vmcnt(0)
	v_add_u32_e32 v17, v17, v13
	s_nop 2
	global_load_dword v14, v1, s[4:5] sc1
	v_readlane_b32 s4, v249, 37
	v_readlane_b32 s5, v249, 38
	s_waitcnt vmcnt(0)
	v_add_u32_e32 v17, v17, v14
	s_nop 2
	global_load_dword v15, v1, s[4:5] sc1
	v_readlane_b32 s4, v249, 39
	v_readlane_b32 s5, v249, 40
	s_waitcnt vmcnt(0)
	v_add_u32_e32 v17, v17, v15
	s_nop 2
	global_load_dword v16, v1, s[4:5] sc1
	s_mov_b64 s[4:5], -1
	s_waitcnt vmcnt(0)
	v_add_u32_e32 v17, v17, v16
	v_cmp_eq_u32_e32 vcc, s9, v17
	s_cbranch_vccnz .LBB0_262
	s_and_b32 s4, s16, 0xff
	s_cmp_eq_u32 s4, 0
	s_mov_b64 s[4:5], -1
	s_mov_b64 s[12:13], -1
	s_sleep 6
	s_cbranch_scc1 .LBB0_267
	s_and_b64 vcc, exec, s[12:13]
	s_cbranch_vccz .LBB0_262

; __device__ __forceinline__ unsigned xb_ld(unsigned* p)              { return __hip_atomic_load(p, __ATOMIC_RELAXED, __HIP_MEMORY_SCOPE_AGENT); }
; __device__ __forceinline__ unsigned xb_add(unsigned* p, unsigned v) { return __hip_atomic_fetch_add(p, v, __ATOMIC_RELAXED, __HIP_MEMORY_SCOPE_AGENT); }
; #define XB_SPIN(cond, bar) do { unsigned _sp = 0; while (cond) { __builtin_amdgcn_s_sleep(1); \
;     if ((++_sp & 255u) == 0u) { if (xb_ld(&(bar)[XB_TMO])) break; if (_sp > XB_SPIN_CAP) { atomicAdd(&(bar)[XB_TMO], 1u); break; } } } } while (0)
; __device__ __forceinline__ void xcd_barrier(const XcdBarrier& b) {
;     ...
;             else XB_SPIN(xb_ld(&bar[XB_TOPGEN]) == tg, bar);
;             __builtin_amdgcn_fence(__ATOMIC_ACQUIRE, "agent");
;             xb_add(&bar[XB_XGEN(b.x)], 1u);
;             asm volatile("s_waitcnt vmcnt(0)" ::: "memory");
;         } else {
;             XB_SPIN(xb_ld(&bar[XB_XGEN(b.x)]) == gen, bar);
.LBB0_281:
	s_and_b32 s16, s9, 0xff
	s_mov_b64 s[40:41], -1
	s_cmp_lg_u32 s16, 0
	s_mov_b64 s[44:45], -1
	s_sleep 6
	s_cbranch_scc0 .LBB0_284
	s_and_b64 vcc, exec, s[44:45]
	s_cbranch_vccz .LBB0_280

; __device__ __forceinline__ unsigned xb_ld(unsigned* p)              { return __hip_atomic_load(p, __ATOMIC_RELAXED, __HIP_MEMORY_SCOPE_AGENT); }
; __device__ __forceinline__ unsigned xb_add(unsigned* p, unsigned v) { return __hip_atomic_fetch_add(p, v, __ATOMIC_RELAXED, __HIP_MEMORY_SCOPE_AGENT); }
; #define XB_SPIN(cond, bar) do { unsigned _sp = 0; while (cond) { __builtin_amdgcn_s_sleep(1); \
;     if ((++_sp & 255u) == 0u) { if (xb_ld(&(bar)[XB_TMO])) break; if (_sp > XB_SPIN_CAP) { atomicAdd(&(bar)[XB_TMO], 1u); break; } } } } while (0)
; __device__ __forceinline__ void xcd_barrier(const XcdBarrier& b) {
;     ...
;             else XB_SPIN(xb_ld(&bar[XB_TOPGEN]) == tg, bar);
;             __builtin_amdgcn_fence(__ATOMIC_ACQUIRE, "agent");
;             xb_add(&bar[XB_XGEN(b.x)], 1u);
;             asm volatile("s_waitcnt vmcnt(0)" ::: "memory");
;         } else {
;             XB_SPIN(xb_ld(&bar[XB_XGEN(b.x)]) == gen, bar);
.LBB0_686:
	s_and_b32 s16, s9, 0xff
	s_mov_b64 s[42:43], -1
	s_cmp_lg_u32 s16, 0
	s_mov_b64 s[46:47], -1
	s_sleep 6
	s_cbranch_scc0 .LBB0_689
	s_and_b64 vcc, exec, s[46:47]
	s_cbranch_vccz .LBB0_685

; __device__ __forceinline__ unsigned xb_ld(unsigned* p)              { return __hip_atomic_load(p, __ATOMIC_RELAXED, __HIP_MEMORY_SCOPE_AGENT); }
; __device__ __forceinline__ void xcd_barrier_complete(unsigned* bar, unsigned x, unsigned& nloc, unsigned& nx) {
;     const unsigned G = gridDim.x * gridDim.y * gridDim.z;
;     unsigned sum, cnt, mine, sp = 0u;
;     for (;;) {
;         sum = 0u; cnt = 0u; mine = 0u;
; #pragma unroll
;         for (unsigned j = 0; j < 16; ++j) { const unsigned c = xb_ld(&bar[XB_XCNT(j)]); sum += c; cnt += (c > 0u) ? 1u : 0u; mine = (j == x) ? c : mine; }
;         if (sum == G) break;
;         __builtin_amdgcn_s_sleep(1);
;         if ((++sp & 255u) == 0u) { if (xb_ld(&bar[XB_TMO])) break; if (sp > XB_SPIN_CAP) { atomicAdd(&bar[XB_TMO], 1u); break; } }
;     }
.LBB0_1304:
	v_readlane_b32 s2, v249, 9
	v_readlane_b32 s3, v249, 10
	s_mov_b64 s[4:5], -1
	s_nop 3
	global_load_dword v0, v1, s[2:3] sc1
	v_readlane_b32 s2, v249, 11
	v_readlane_b32 s3, v249, 12
	s_nop 4
	global_load_dword v2, v1, s[2:3] sc1
	v_readlane_b32 s2, v249, 13
	v_readlane_b32 s3, v249, 14
	s_waitcnt vmcnt(0)
	v_add_u32_e32 v17, v2, v0
	s_nop 2
	global_load_dword v3, v1, s[2:3] sc1
	v_readlane_b32 s2, v249, 15
	v_readlane_b32 s3, v249, 16
	s_waitcnt vmcnt(0)
	v_add_u32_e32 v17, v17, v3
	s_nop 2
	global_load_dword v4, v1, s[2:3] sc1
	v_readlane_b32 s2, v249, 17
	v_readlane_b32 s3, v249, 18
	s_waitcnt vmcnt(0)
	v_add_u32_e32 v17, v17, v4
	s_nop 2
	global_load_dword v5, v1, s[2:3] sc1
	v_readlane_b32 s2, v249, 19
	v_readlane_b32 s3, v249, 20
	s_waitcnt vmcnt(0)
	v_add_u32_e32 v17, v17, v5
	s_nop 2
	global_load_dword v6, v1, s[2:3] sc1
	v_readlane_b32 s2, v249, 21
	v_readlane_b32 s3, v249, 22
	s_waitcnt vmcnt(0)
	v_add_u32_e32 v17, v17, v6
	s_nop 2
	global_load_dword v7, v1, s[2:3] sc1
	v_readlane_b32 s2, v249, 23
	v_readlane_b32 s3, v249, 24
	s_waitcnt vmcnt(0)
	v_add_u32_e32 v17, v17, v7
	s_nop 2
	global_load_dword v8, v1, s[2:3] sc1
	v_readlane_b32 s2, v249, 25
	v_readlane_b32 s3, v249, 26
	s_waitcnt vmcnt(0)
	v_add_u32_e32 v17, v17, v8
	s_nop 2
	global_load_dword v9, v1, s[2:3] sc1
	v_readlane_b32 s2, v249, 27
	v_readlane_b32 s3, v249, 28
	s_waitcnt vmcnt(0)
	v_add_u32_e32 v17, v17, v9
	s_nop 2
	global_load_dword v10, v1, s[2:3] sc1
	v_readlane_b32 s2, v249, 29
	v_readlane_b32 s3, v249, 30
	s_waitcnt vmcnt(0)
	v_add_u32_e32 v17, v17, v10
	s_nop 2
	global_load_dword v11, v1, s[2:3] sc1
	v_readlane_b32 s2, v249, 31
	v_readlane_b32 s3, v249, 32
	s_waitcnt vmcnt(0)
	v_add_u32_e32 v17, v17, v11
	s_nop 2
	global_load_dword v12, v1, s[2:3] sc1
	v_readlane_b32 s2, v249, 33
	v_readlane_b32 s3, v249, 34
	s_waitcnt vmcnt(0)
	v_add_u32_e32 v17, v17, v12
	s_nop 2
	global_load_dword v13, v1, s[2:3] sc1
	v_readlane_b32 s2, v249, 35
	v_readlane_b32 s3, v249, 36
	s_waitcnt vmcnt(0)
	v_add_u32_e32 v17, v17, v13
	s_nop 2
	global_load_dword v14, v1, s[2:3] sc1
	v_readlane_b32 s2, v249, 37
	v_readlane_b32 s3, v249, 38
	s_waitcnt vmcnt(0)
	v_add_u32_e32 v17, v17, v14
	s_nop 2
	global_load_dword v15, v1, s[2:3] sc1
	v_readlane_b32 s2, v249, 39
	v_readlane_b32 s3, v249, 40
	s_waitcnt vmcnt(0)
	v_add_u32_e32 v17, v17, v15
	s_nop 2
	global_load_dword v16, v1, s[2:3] sc1
	s_mov_b64 s[2:3], -1
	s_waitcnt vmcnt(0)
	v_add_u32_e32 v17, v17, v16
	v_cmp_eq_u32_e32 vcc, s8, v17
	s_cbranch_vccnz .LBB0_1303
	s_and_b32 s2, s9, 0xff
	s_cmp_eq_u32 s2, 0
	s_mov_b64 s[2:3], -1
	s_mov_b64 s[10:11], -1
	s_sleep 6
	s_cbranch_scc1 .LBB0_1308
	s_and_b64 vcc, exec, s[10:11]
	s_cbranch_vccz .LBB0_1303

; __device__ __forceinline__ unsigned xb_ld(unsigned* p)              { return __hip_atomic_load(p, __ATOMIC_RELAXED, __HIP_MEMORY_SCOPE_AGENT); }
; __device__ __forceinline__ unsigned xb_add(unsigned* p, unsigned v) { return __hip_atomic_fetch_add(p, v, __ATOMIC_RELAXED, __HIP_MEMORY_SCOPE_AGENT); }
; #define XB_SPIN(cond, bar) do { unsigned _sp = 0; while (cond) { __builtin_amdgcn_s_sleep(1); \
;     if ((++_sp & 255u) == 0u) { if (xb_ld(&(bar)[XB_TMO])) break; if (_sp > XB_SPIN_CAP) { atomicAdd(&(bar)[XB_TMO], 1u); break; } } } } while (0)
; __device__ __forceinline__ void xcd_barrier(const XcdBarrier& b) {
;     ...
;             else XB_SPIN(xb_ld(&bar[XB_TOPGEN]) == tg, bar);
;             __builtin_amdgcn_fence(__ATOMIC_ACQUIRE, "agent");
;             xb_add(&bar[XB_XGEN(b.x)], 1u);
;             asm volatile("s_waitcnt vmcnt(0)" ::: "memory");
;         } else {
;             XB_SPIN(xb_ld(&bar[XB_XGEN(b.x)]) == gen, bar);
.LBB0_1322:
	s_and_b32 s9, s8, 0xff
	s_mov_b64 s[38:39], -1
	s_cmp_lg_u32 s9, 0
	s_mov_b64 s[42:43], -1
	s_sleep 6
	s_cbranch_scc0 .LBB0_1325
	s_and_b64 vcc, exec, s[42:43]
	s_cbranch_vccz .LBB0_1321
